# SCAN1 software prefetch: next sub-chunk's 8 first-half vector loads issued one trip ahead into spare VGPRs, second-half loads hoisted to trip top; in-loop vmcnt waits reduced to two
# baseline (speedup 1.0000x reference)
.LBB0_1290:
	v_mov_b32_e32 v212, v1
	s_add_u32 s28, s41, s26
	s_addc_u32 s29, s42, s27
	v_and_b32_e32 v144, 15, v212
	v_and_b32_e32 v148, -16, v212
	v_lshl_add_u64 v[130:131], s[28:29], 0, v[144:145]
	v_ashrrev_i32_e32 v149, 31, v148
	v_lshlrev_b64 v[130:131], 10, v[130:131]
	v_lshl_add_u64 v[132:133], v[148:149], 0, s[6:7]
	v_lshl_add_u64 v[130:131], v[132:133], 0, v[130:131]
	v_lshlrev_b64 v[142:143], 1, v[130:131]
	v_lshl_add_u64 v[146:147], s[8:9], 0, v[142:143]
	s_cmp_lg_u32 s26, 0
	s_cbranch_scc1 .Lsc1_havepf
	v_lshl_add_u64 v[218:219], s[8:9], 0, v[142:143]
	global_load_dwordx4 v[218:221], v[218:219], off
	v_lshl_add_u64 v[222:223], s[14:15], 0, v[142:143]
	global_load_dwordx4 v[222:225], v[222:223], off
	v_lshl_add_u64 v[226:227], s[14:15], 0, v[142:143]
	global_load_dwordx4 v[226:229], v[226:227], off offset:16
	v_lshl_add_u64 v[230:231], s[16:17], 0, v[142:143]
	global_load_dwordx4 v[230:233], v[230:231], off
	v_lshl_add_u64 v[234:235], s[18:19], 0, v[142:143]
	global_load_dwordx4 v[234:237], v[234:235], off
	v_lshl_add_u64 v[238:239], s[20:21], 0, v[142:143]
	global_load_dwordx4 v[238:241], v[238:239], off
	v_lshl_add_u64 v[242:243], s[8:9], 0, v[142:143]
	global_load_dwordx4 v[242:245], v[242:243], off offset:16
	v_lshl_add_u64 v[246:247], s[22:23], 0, v[142:143]
	global_load_dwordx4 v[246:249], v[246:247], off
.Lsc1_havepf:
	s_waitcnt vmcnt(0)
	v_mov_b32_e32 v130, v218
	v_mov_b32_e32 v131, v219
	v_mov_b32_e32 v132, v220
	v_mov_b32_e32 v133, v221

	v_mov_b32_e32 v134, v222
	v_mov_b32_e32 v135, v223
	v_mov_b32_e32 v136, v224
	v_mov_b32_e32 v137, v225
	s_nop 0
	v_mov_b32_e32 v138, v226
	v_mov_b32_e32 v139, v227
	v_mov_b32_e32 v140, v228
	v_mov_b32_e32 v141, v229
	v_lshl_add_u64 v[218:219], s[16:17], 0, v[142:143]
	global_load_dwordx4 v[218:221], v[218:219], off offset:16
	v_lshl_add_u64 v[222:223], s[18:19], 0, v[142:143]
	global_load_dwordx4 v[222:225], v[222:223], off offset:16
	v_lshl_add_u64 v[226:227], s[20:21], 0, v[142:143]
	global_load_dwordx4 v[226:229], v[226:227], off offset:16
	v_lshl_add_u64 v[250:251], s[22:23], 0, v[142:143]
	global_load_dwordx4 v[250:253], v[250:251], off offset:16
	v_ashrrev_i32_e32 v179, 4, v212
	v_lshlrev_b32_e32 v178, 9, v179
	v_lshlrev_b32_e32 v180, 5, v144
	v_add3_u32 v149, s36, v178, v180
	v_mov_b32_e32 v161, 0
	v_cmp_eq_u32_e32 vcc, 15, v144
	s_mov_b64 s[96:97], vcc
	v_lshl_add_u32 v181, v148, 2, s36
	v_lshl_add_u32 v255, v148, 2, s36

	ds_write_b128 v149, v[134:137] offset:12288

	ds_write_b128 v149, v[138:141] offset:12304
	v_cvt_f32_f16_e32 v155, v130
	s_nop 1
	v_add_f32_dpp v134, v155, v155 row_shr:1 row_mask:0xf bank_mask:0xf bound_ctrl:1
	s_nop 0
	s_nop 0
	v_add_f32_dpp v134, v134, v134 row_shr:2 row_mask:0xf bank_mask:0xf bound_ctrl:1
	s_nop 0
	s_nop 0
	v_add_f32_dpp v172, v134, v134 row_shr:4 row_mask:0xf bank_mask:0xf bound_ctrl:1
	s_nop 0
	s_nop 0
	v_mov_b32_dpp v161, v172 row_shr:8 row_mask:0xf bank_mask:0xf
	s_nop 0


	v_cvt_f32_f16_sdwa v130, v130 dst_sel:DWORD dst_unused:UNUSED_PAD src0_sel:WORD_1
	v_mov_b32_e32 v148, 0
	s_nop 0
	v_add_f32_dpp v134, v130, v130 row_shr:1 row_mask:0xf bank_mask:0xf bound_ctrl:1
	s_nop 0
	s_nop 0
	v_add_f32_dpp v134, v134, v134 row_shr:2 row_mask:0xf bank_mask:0xf bound_ctrl:1
	s_nop 1
	v_add_f32_dpp v173, v134, v134 row_shr:4 row_mask:0xf bank_mask:0xf bound_ctrl:1
	s_nop 0
	s_nop 0
	v_mov_b32_dpp v148, v173 row_shr:8 row_mask:0xf bank_mask:0xf
	s_nop 0
	s_nop 1
	s_nop 0


	v_cvt_f32_f16_e32 v174, v131
	v_mov_b32_e32 v168, 0
	s_nop 0
	v_add_f32_dpp v134, v174, v174 row_shr:1 row_mask:0xf bank_mask:0xf bound_ctrl:1
	s_nop 0
	s_nop 0
	v_add_f32_dpp v134, v134, v134 row_shr:2 row_mask:0xf bank_mask:0xf bound_ctrl:1
	s_nop 1
	v_add_f32_dpp v177, v134, v134 row_shr:4 row_mask:0xf bank_mask:0xf bound_ctrl:1
	s_nop 0
	s_nop 0
	v_mov_b32_dpp v168, v177 row_shr:8 row_mask:0xf bank_mask:0xf
	s_nop 0
	s_nop 1
	s_nop 0


	v_cvt_f32_f16_sdwa v131, v131 dst_sel:DWORD dst_unused:UNUSED_PAD src0_sel:WORD_1
	v_mov_b32_e32 v166, 0
	s_nop 0
	v_add_f32_dpp v134, v131, v131 row_shr:1 row_mask:0xf bank_mask:0xf bound_ctrl:1
	s_nop 0
	s_nop 0
	v_add_f32_dpp v134, v134, v134 row_shr:2 row_mask:0xf bank_mask:0xf bound_ctrl:1
	s_nop 1
	v_add_f32_dpp v169, v134, v134 row_shr:4 row_mask:0xf bank_mask:0xf bound_ctrl:1
	s_nop 0
	s_nop 0
	v_mov_b32_dpp v166, v169 row_shr:8 row_mask:0xf bank_mask:0xf
	s_nop 0
	s_nop 1
	s_nop 0


	v_cvt_f32_f16_e32 v138, v132
	v_mov_b32_e32 v139, 0
	s_nop 0
	v_add_f32_dpp v134, v138, v138 row_shr:1 row_mask:0xf bank_mask:0xf bound_ctrl:1
	s_nop 0
	s_nop 0
	v_add_f32_dpp v134, v134, v134 row_shr:2 row_mask:0xf bank_mask:0xf bound_ctrl:1
	s_nop 1
	v_add_f32_dpp v141, v134, v134 row_shr:4 row_mask:0xf bank_mask:0xf bound_ctrl:1
	s_nop 0
	s_nop 0
	v_mov_b32_dpp v139, v141 row_shr:8 row_mask:0xf bank_mask:0xf
	s_nop 0
	s_nop 1
	s_nop 0


	v_cvt_f32_f16_sdwa v150, v132 dst_sel:DWORD dst_unused:UNUSED_PAD src0_sel:WORD_1
	v_mov_b32_e32 v134, 0
	s_nop 0
	v_add_f32_dpp v132, v150, v150 row_shr:1 row_mask:0xf bank_mask:0xf bound_ctrl:1
	s_nop 0
	s_nop 0
	v_add_f32_dpp v132, v132, v132 row_shr:2 row_mask:0xf bank_mask:0xf bound_ctrl:1
	s_nop 1
	v_add_f32_dpp v135, v132, v132 row_shr:4 row_mask:0xf bank_mask:0xf bound_ctrl:1
	s_nop 0
	s_nop 0
	v_mov_b32_dpp v134, v135 row_shr:8 row_mask:0xf bank_mask:0xf
	s_nop 0
	s_nop 1
	s_nop 0


	v_cvt_f32_f16_e32 v136, v133
	v_mov_b32_e32 v137, 0
	s_nop 0
	v_add_f32_dpp v132, v136, v136 row_shr:1 row_mask:0xf bank_mask:0xf bound_ctrl:1
	s_nop 0
	s_nop 0
	v_add_f32_dpp v132, v132, v132 row_shr:2 row_mask:0xf bank_mask:0xf bound_ctrl:1
	s_nop 1
	v_add_f32_dpp v153, v132, v132 row_shr:4 row_mask:0xf bank_mask:0xf bound_ctrl:1
	s_nop 0
	s_nop 0
	v_mov_b32_dpp v137, v153 row_shr:8 row_mask:0xf bank_mask:0xf
	s_nop 0
	s_nop 1
	s_nop 0


	v_cvt_f32_f16_sdwa v132, v133 dst_sel:DWORD dst_unused:UNUSED_PAD src0_sel:WORD_1
	v_mov_b32_e32 v156, 0
	s_nop 0
	v_add_f32_dpp v133, v132, v132 row_shr:1 row_mask:0xf bank_mask:0xf bound_ctrl:1
	s_nop 0
	s_nop 0
	v_add_f32_dpp v133, v133, v133 row_shr:2 row_mask:0xf bank_mask:0xf bound_ctrl:1
	s_nop 1
	v_add_f32_dpp v157, v133, v133 row_shr:4 row_mask:0xf bank_mask:0xf bound_ctrl:1
	s_nop 0
	s_nop 0
	v_mov_b32_dpp v156, v157 row_shr:8 row_mask:0xf bank_mask:0xf
	s_nop 0
	s_nop 1
	s_nop 0


	v_add_f32_e32 v137, v153, v137
	s_nop 1
	v_mov_b32_dpp v152, v137 row_newbcast:15 row_mask:0xf bank_mask:0xf
	v_sub_f32_e32 v136, v137, v136
	v_mul_f32_e32 v153, 0x3fb8aa3b, v137
	v_mul_f32_e32 v136, 0x3fb8aa3b, v136
	v_exp_f32_e32 v154, v153
	s_mov_b64 exec, s[96:97]
	ds_write_b32 v255, v154 offset:16408
	s_mov_b64 exec, -1
	v_mul_f32_e32 v153, 0xbfb8aa3b, v137
	v_exp_f32_e32 v162, v136
	v_sub_f32_e32 v136, v152, v137
	v_add_f32_e32 v188, v157, v156
	s_nop 1
	v_mov_b32_dpp v133, v188 row_newbcast:15 row_mask:0xf bank_mask:0xf
	v_add_f32_e32 v156, v135, v134
	s_nop 1
	v_mov_b32_dpp v151, v156 row_newbcast:15 row_mask:0xf bank_mask:0xf
	v_exp_f32_e32 v159, v153
	v_mul_f32_e32 v136, 0x3fb8aa3b, v136
	v_mul_f32_e32 v134, 0x3fb8aa3b, v156
	v_lshl_add_u64 v[152:153], s[16:17], 0, v[142:143]
	v_exp_f32_e32 v160, v136
	v_exp_f32_e32 v157, v134
	s_mov_b64 exec, s[96:97]
	ds_write_b32 v255, v157 offset:16404
	s_mov_b64 exec, -1
	v_mov_b32_e32 v134, v230
	v_mov_b32_e32 v135, v231
	v_mov_b32_e32 v136, v232
	v_mov_b32_e32 v137, v233
	v_sub_f32_e32 v150, v156, v150
	v_mul_f32_e32 v150, 0x3fb8aa3b, v150
	v_add_f32_e32 v139, v141, v139
	s_nop 1
	v_mov_b32_dpp v140, v139 row_newbcast:15 row_mask:0xf bank_mask:0xf
	v_exp_f32_e32 v171, v150
	v_sub_f32_e32 v150, v151, v156
	v_sub_f32_e32 v138, v139, v138
	v_mul_f32_e32 v150, 0x3fb8aa3b, v150
	v_mul_f32_e32 v141, 0x3fb8aa3b, v139
	v_mul_f32_e32 v138, 0x3fb8aa3b, v138
	v_mul_f32_e32 v158, 0xbfb8aa3b, v156
	v_exp_f32_e32 v165, v150
	v_exp_f32_e32 v156, v141
	s_mov_b64 exec, s[96:97]
	ds_write_b32 v255, v156 offset:16400
	s_mov_b64 exec, -1
	v_mul_f32_e32 v141, 0xbfb8aa3b, v139
	v_exp_f32_e32 v170, v138
	v_sub_f32_e32 v138, v140, v139
	v_lshl_add_u64 v[150:151], s[18:19], 0, v[142:143]
	v_exp_f32_e32 v167, v141
	v_mul_f32_e32 v164, 0x3fb8aa3b, v138
	v_mov_b32_e32 v138, v234
	v_mov_b32_e32 v139, v235
	v_mov_b32_e32 v140, v236
	v_mov_b32_e32 v141, v237
	v_add_f32_e32 v182, v169, v166
	s_nop 1
	v_mov_b32_dpp v175, v182 row_newbcast:15 row_mask:0xf bank_mask:0xf
	v_sub_f32_e32 v131, v182, v131
	v_mul_f32_e32 v131, 0x3fb8aa3b, v131
	v_exp_f32_e32 v191, v131
	v_sub_f32_e32 v131, v175, v182
	v_mul_f32_e32 v131, 0x3fb8aa3b, v131
	v_exp_f32_e32 v175, v131
	v_add_f32_e32 v131, v177, v168
	s_nop 1
	v_mov_b32_dpp v176, v131 row_newbcast:15 row_mask:0xf bank_mask:0xf
	v_mul_f32_e32 v168, 0x3fb8aa3b, v131
	v_mul_f32_e32 v177, 0xbfb8aa3b, v131
	v_sub_f32_e32 v174, v131, v174
	v_sub_f32_e32 v131, v176, v131
	v_mul_f32_e32 v174, 0x3fb8aa3b, v174
	v_mul_f32_e32 v131, 0x3fb8aa3b, v131
	v_exp_f32_e32 v190, v174
	v_exp_f32_e32 v174, v131
	v_add_f32_e32 v131, v173, v148
	s_nop 1
	v_mov_b32_dpp v149, v131 row_newbcast:15 row_mask:0xf bank_mask:0xf
	v_mul_f32_e32 v148, 0x3fb8aa3b, v131
	v_sub_f32_e32 v130, v131, v130
	v_exp_f32_e32 v173, v148
	s_mov_b64 exec, s[96:97]
	ds_write_b32 v255, v173 offset:16388
	s_mov_b64 exec, -1
	v_mul_f32_e32 v148, 0xbfb8aa3b, v131
	v_mul_f32_e32 v130, 0x3fb8aa3b, v130
	v_mul_f32_e32 v166, 0x3fb8aa3b, v182
	v_exp_f32_e32 v176, v148
	v_exp_f32_e32 v187, v130
	v_sub_f32_e32 v130, v149, v131
	v_lshl_add_u64 v[148:149], s[20:21], 0, v[142:143]
	v_exp_f32_e32 v169, v166
	s_mov_b64 exec, s[96:97]
	ds_write_b32 v255, v169 offset:16396
	s_mov_b64 exec, -1
	v_mul_f32_e32 v166, 0xbfb8aa3b, v182
	v_mov_b32_e32 v182, v238
	v_mov_b32_e32 v183, v239
	v_mov_b32_e32 v184, v240
	v_mov_b32_e32 v185, v241
	v_mul_f32_e32 v130, 0x3fb8aa3b, v130
	v_exp_f32_e32 v195, v130
	v_add_f32_e32 v130, v172, v161
	s_nop 1
	v_mov_b32_dpp v163, v130 row_newbcast:15 row_mask:0xf bank_mask:0xf
	v_mul_f32_e32 v131, 0x3fb8aa3b, v130
	v_exp_f32_e32 v172, v131
	s_mov_b64 exec, s[96:97]
	ds_write_b32 v255, v172 offset:16384
	s_mov_b64 exec, -1
	v_mul_f32_e32 v131, 0xbfb8aa3b, v130
	v_exp_f32_e32 v196, v131
	v_sub_f32_e32 v131, v130, v155
	v_sub_f32_e32 v130, v163, v130
	v_mul_f32_e32 v130, 0x3fb8aa3b, v130
	v_exp_f32_e32 v194, v130
	v_mul_f32_e32 v130, 0x3fb8aa3b, v188
	v_exp_f32_e32 v155, v130
	s_mov_b64 exec, s[96:97]
	ds_write_b32 v255, v155 offset:16412
	s_mov_b64 exec, -1
	v_mul_f32_e32 v130, 0xbfb8aa3b, v188
	v_exp_f32_e32 v198, v130
	v_sub_f32_e32 v130, v188, v132
	v_mul_f32_e32 v130, 0x3fb8aa3b, v130
	v_mul_f32_e32 v131, 0x3fb8aa3b, v131
	v_exp_f32_e32 v163, v130
	v_sub_f32_e32 v130, v133, v188
	v_exp_f32_e32 v186, v131
	v_mul_f32_e32 v161, 0x3fb8aa3b, v130
	v_mov_b32_e32 v130, v242
	v_mov_b32_e32 v131, v243
	v_mov_b32_e32 v132, v244
	v_mov_b32_e32 v133, v245
	v_lshl_add_u64 v[142:143], s[22:23], 0, v[142:143]
	v_or_b32_e32 v197, v180, v178
	v_exp_f32_e32 v177, v177
	v_exp_f32_e32 v166, v166
	v_exp_f32_e32 v164, v164
	v_exp_f32_e32 v158, v158
	v_exp_f32_e32 v161, v161

	v_cvt_f32_f16_e32 v146, v134
	v_cvt_f32_f16_sdwa v147, v134 dst_sel:DWORD dst_unused:UNUSED_PAD src0_sel:WORD_1
	v_cvt_f32_f16_e32 v192, v135
	v_cvt_f32_f16_sdwa v193, v135 dst_sel:DWORD dst_unused:UNUSED_PAD src0_sel:WORD_1
	v_exp_f32_e32 v168, v168
	s_mov_b64 exec, s[96:97]
	ds_write_b32 v255, v168 offset:16392
	s_mov_b64 exec, -1
	v_mul_f32_e32 v134, v186, v146
	v_mul_f32_e32 v135, v187, v147
	v_mov_b32_e32 v186, v246
	v_mov_b32_e32 v187, v247
	v_mov_b32_e32 v188, v248
	v_mov_b32_e32 v189, v249
	v_mul_f32_e32 v146, v190, v192
	v_mul_f32_e32 v147, v191, v193
	v_cvt_f32_f16_e32 v190, v136
	v_cvt_f32_f16_sdwa v191, v136 dst_sel:DWORD dst_unused:UNUSED_PAD src0_sel:WORD_1
	v_cvt_f32_f16_e32 v192, v137
	v_cvt_f32_f16_sdwa v193, v137 dst_sel:DWORD dst_unused:UNUSED_PAD src0_sel:WORD_1
	v_cvt_pk_f16_f32 v134, v134, v135
	v_cvt_pk_f16_f32 v135, v146, v147
	v_mul_f32_e32 v136, v170, v190
	v_mul_f32_e32 v137, v171, v191
	v_mul_f32_e32 v146, v162, v192
	v_mul_f32_e32 v147, v163, v193
	v_cvt_pk_f16_f32 v136, v136, v137
	v_cvt_pk_f16_f32 v137, v146, v147
	v_add_u32_e32 v147, s36, v197
	ds_write_b128 v147, v[134:137]

	v_cvt_f32_f16_e32 v136, v138
	v_cvt_f32_f16_sdwa v137, v138 dst_sel:DWORD dst_unused:UNUSED_PAD src0_sel:WORD_1
	v_cvt_f32_f16_e32 v162, v139
	v_cvt_f32_f16_sdwa v163, v139 dst_sel:DWORD dst_unused:UNUSED_PAD src0_sel:WORD_1
	v_fma_mixlo_f16 v146, v196, v138, 0 op_sel_hi:[0,1,0]
	v_cvt_f32_f16_e32 v138, v140
	v_cvt_f32_f16_sdwa v139, v140 dst_sel:DWORD dst_unused:UNUSED_PAD src0_sel:WORD_1
	v_mul_f32_e32 v134, v194, v136
	v_mul_f32_e32 v135, v195, v137
	v_mov_b32_e32 v136, v137
	v_mov_b32_e32 v137, v162
	v_cvt_pk_f16_f32 v134, v134, v135
	v_mul_f32_e32 v136, v176, v136
	v_mul_f32_e32 v137, v177, v137
	s_nop 0
	v_cvt_pk_f16_f32 v170, v136, v137
	v_mul_f32_e32 v136, v174, v162
	v_mul_f32_e32 v137, v175, v163
	v_pack_b32_f16 v190, v146, v170
	v_cvt_pk_f16_f32 v135, v136, v137
	v_mov_b32_e32 v136, v163
	v_mov_b32_e32 v137, v138
	v_cvt_f32_f16_e32 v162, v141
	v_cvt_f32_f16_sdwa v163, v141 dst_sel:DWORD dst_unused:UNUSED_PAD src0_sel:WORD_1
	v_mul_f32_e32 v136, v166, v136
	v_mul_f32_e32 v137, v167, v137
	s_nop 0
	v_cvt_pk_f16_f32 v140, v136, v137
	v_mul_f32_e32 v136, v164, v138
	v_mul_f32_e32 v137, v165, v139
	v_mov_b32_e32 v138, v139
	v_mov_b32_e32 v139, v162
	v_cvt_pk_f16_f32 v136, v136, v137
	v_mul_f32_e32 v138, v158, v138
	v_mul_f32_e32 v139, v159, v139
	v_alignbit_b32 v191, v140, v170, 16
	v_cvt_pk_f16_f32 v137, v138, v139
	v_lshrrev_b32_e32 v193, 16, v137
	v_mul_f32_e32 v138, v160, v162
	v_mul_f32_e32 v139, v161, v163
	v_alignbit_b32 v192, v137, v140, 16
	v_cvt_pk_f16_f32 v137, v138, v139
	v_fma_mixhi_f16 v193, v198, v141, 0 op_sel:[0,1,0] op_sel_hi:[0,1,0]
	ds_write_b128 v147, v[190:193] offset:2048
	ds_write_b128 v147, v[134:137] offset:8192

	v_cvt_f32_f16_e32 v136, v182
	v_cvt_f32_f16_sdwa v137, v182 dst_sel:DWORD dst_unused:UNUSED_PAD src0_sel:WORD_1
	v_cvt_f32_f16_e32 v140, v183
	v_cvt_f32_f16_sdwa v141, v183 dst_sel:DWORD dst_unused:UNUSED_PAD src0_sel:WORD_1
	v_cvt_f32_f16_e32 v162, v184
	v_cvt_f32_f16_sdwa v163, v184 dst_sel:DWORD dst_unused:UNUSED_PAD src0_sel:WORD_1
	v_mul_f32_e32 v134, v194, v136
	v_mul_f32_e32 v135, v195, v137
	v_mov_b32_e32 v136, v137
	v_mov_b32_e32 v137, v140
	v_cvt_pk_f16_f32 v134, v134, v135
	v_mul_f32_e32 v136, v176, v136
	v_mul_f32_e32 v137, v177, v137
	v_fma_mixlo_f16 v138, v196, v182, 0 op_sel_hi:[0,1,0]
	v_cvt_pk_f16_f32 v139, v136, v137
	v_mul_f32_e32 v136, v174, v140
	v_mul_f32_e32 v137, v175, v141
	v_pack_b32_f16 v138, v138, v139
	v_cvt_pk_f16_f32 v135, v136, v137
	v_mov_b32_e32 v136, v141
	v_mov_b32_e32 v137, v162
	s_nop 0
	v_mul_f32_e32 v136, v166, v136
	v_mul_f32_e32 v137, v167, v137
	v_cvt_f32_f16_e32 v166, v185
	v_cvt_f32_f16_sdwa v167, v185 dst_sel:DWORD dst_unused:UNUSED_PAD src0_sel:WORD_1
	v_cvt_pk_f16_f32 v146, v136, v137
	v_mul_f32_e32 v136, v164, v162
	v_mul_f32_e32 v137, v165, v163
	v_alignbit_b32 v139, v146, v139, 16
	v_mov_b32_e32 v140, v163
	v_mov_b32_e32 v141, v166
	v_cvt_pk_f16_f32 v136, v136, v137
	v_mul_f32_e32 v140, v158, v140
	v_mul_f32_e32 v141, v159, v141
	v_mul_f32_e32 v158, v160, v166
	v_mul_f32_e32 v159, v161, v167
	v_cvt_pk_f16_f32 v137, v140, v141
	v_lshrrev_b32_e32 v141, 16, v137
	v_alignbit_b32 v140, v137, v146, 16
	v_fma_mixhi_f16 v141, v198, v185, 0 op_sel:[0,1,0] op_sel_hi:[0,1,0]
	ds_write_b128 v147, v[138:141] offset:4096

	v_cvt_f32_f16_e32 v138, v186
	v_cvt_f32_f16_sdwa v139, v186 dst_sel:DWORD dst_unused:UNUSED_PAD src0_sel:WORD_1
	v_cvt_pk_f16_f32 v137, v158, v159
	v_cvt_f32_f16_e32 v140, v187
	v_cvt_f32_f16_sdwa v141, v187 dst_sel:DWORD dst_unused:UNUSED_PAD src0_sel:WORD_1
	ds_write_b128 v147, v[134:137] offset:10240
	v_cvt_f32_f16_e32 v136, v188
	v_cvt_f32_f16_sdwa v137, v188 dst_sel:DWORD dst_unused:UNUSED_PAD src0_sel:WORD_1
	v_mul_f32_e32 v134, v172, v138
	v_mul_f32_e32 v135, v173, v139
	v_mul_f32_e32 v136, v156, v136
	v_mul_f32_e32 v137, v157, v137
	v_cvt_pk_f16_f32 v138, v134, v135
	v_mul_f32_e32 v134, v168, v140
	v_mul_f32_e32 v135, v169, v141
	v_cvt_pk_f16_f32 v140, v136, v137
	v_cvt_pk_f16_f32 v139, v134, v135
	v_cvt_f32_f16_e32 v134, v189
	v_cvt_f32_f16_sdwa v135, v189 dst_sel:DWORD dst_unused:UNUSED_PAD src0_sel:WORD_1
	v_cvt_f32_f16_e32 v137, v130
	v_mul_f32_e32 v134, v154, v134
	v_mul_f32_e32 v135, v155, v135
	s_nop 0
	v_cvt_pk_f16_f32 v141, v134, v135
	v_add_f32_dpp v134, v137, v137 row_shr:1 row_mask:0xf bank_mask:0xf bound_ctrl:1
	ds_write_b128 v147, v[138:141] offset:6144
	v_mov_b32_e32 v154, 0
	v_add_f32_dpp v134, v134, v134 row_shr:2 row_mask:0xf bank_mask:0xf bound_ctrl:1
	s_nop 1
	v_add_f32_dpp v139, v134, v134 row_shr:4 row_mask:0xf bank_mask:0xf bound_ctrl:1
	s_nop 0
	s_nop 0
	v_mov_b32_dpp v154, v139 row_shr:8 row_mask:0xf bank_mask:0xf
	s_nop 0
	s_nop 1
	s_nop 0
	s_nop 1
	s_nop 0


	v_cvt_f32_f16_sdwa v156, v130 dst_sel:DWORD dst_unused:UNUSED_PAD src0_sel:WORD_1
	v_mov_b32_e32 v158, 0
	s_nop 0
	v_add_f32_dpp v130, v156, v156 row_shr:1 row_mask:0xf bank_mask:0xf bound_ctrl:1
	s_nop 0
	s_nop 0
	v_add_f32_dpp v130, v130, v130 row_shr:2 row_mask:0xf bank_mask:0xf bound_ctrl:1
	s_nop 1
	v_add_f32_dpp v159, v130, v130 row_shr:4 row_mask:0xf bank_mask:0xf bound_ctrl:1
	s_nop 0
	s_nop 0
	v_mov_b32_dpp v158, v159 row_shr:8 row_mask:0xf bank_mask:0xf
	s_nop 0
	s_nop 1
	s_nop 0


	v_cvt_f32_f16_e32 v160, v131
	v_mov_b32_e32 v161, 0
	s_nop 0
	v_add_f32_dpp v130, v160, v160 row_shr:1 row_mask:0xf bank_mask:0xf bound_ctrl:1
	s_nop 0
	s_nop 0
	v_add_f32_dpp v130, v130, v130 row_shr:2 row_mask:0xf bank_mask:0xf bound_ctrl:1
	s_nop 1
	v_add_f32_dpp v163, v130, v130 row_shr:4 row_mask:0xf bank_mask:0xf bound_ctrl:1
	s_nop 0
	s_nop 0
	v_mov_b32_dpp v161, v163 row_shr:8 row_mask:0xf bank_mask:0xf
	s_nop 0
	s_nop 1
	s_nop 0


	v_cvt_f32_f16_sdwa v131, v131 dst_sel:DWORD dst_unused:UNUSED_PAD src0_sel:WORD_1
	v_mov_b32_e32 v165, 0
	s_nop 0
	v_add_f32_dpp v130, v131, v131 row_shr:1 row_mask:0xf bank_mask:0xf bound_ctrl:1
	s_nop 0
	s_nop 0
	v_add_f32_dpp v130, v130, v130 row_shr:2 row_mask:0xf bank_mask:0xf bound_ctrl:1
	s_nop 1
	v_add_f32_dpp v167, v130, v130 row_shr:4 row_mask:0xf bank_mask:0xf bound_ctrl:1
	s_nop 0
	s_nop 0
	v_mov_b32_dpp v165, v167 row_shr:8 row_mask:0xf bank_mask:0xf
	s_nop 0
	s_nop 1
	s_nop 0


	v_cvt_f32_f16_e32 v140, v132
	v_mov_b32_e32 v134, 0
	s_nop 0
	v_add_f32_dpp v130, v140, v140 row_shr:1 row_mask:0xf bank_mask:0xf bound_ctrl:1
	s_nop 0
	s_nop 0
	v_add_f32_dpp v130, v130, v130 row_shr:2 row_mask:0xf bank_mask:0xf bound_ctrl:1
	s_nop 1
	v_add_f32_dpp v170, v130, v130 row_shr:4 row_mask:0xf bank_mask:0xf bound_ctrl:1
	s_nop 0
	s_nop 0
	v_mov_b32_dpp v134, v170 row_shr:8 row_mask:0xf bank_mask:0xf
	s_nop 0
	s_nop 1
	s_nop 0


	v_cvt_f32_f16_sdwa v141, v132 dst_sel:DWORD dst_unused:UNUSED_PAD src0_sel:WORD_1
	v_mov_b32_e32 v132, 0
	s_nop 0
	v_add_f32_dpp v130, v141, v141 row_shr:1 row_mask:0xf bank_mask:0xf bound_ctrl:1
	s_nop 0
	s_nop 0
	v_add_f32_dpp v130, v130, v130 row_shr:2 row_mask:0xf bank_mask:0xf bound_ctrl:1
	s_nop 1
	v_add_f32_dpp v135, v130, v130 row_shr:4 row_mask:0xf bank_mask:0xf bound_ctrl:1
	s_nop 0
	s_nop 0
	v_mov_b32_dpp v132, v135 row_shr:8 row_mask:0xf bank_mask:0xf
	s_nop 0
	s_nop 1
	s_nop 0


	v_cvt_f32_f16_e32 v136, v133
	v_mov_b32_e32 v130, 0
	s_nop 0
	v_add_f32_dpp v138, v136, v136 row_shr:1 row_mask:0xf bank_mask:0xf bound_ctrl:1
	s_nop 0
	s_nop 0
	v_add_f32_dpp v138, v138, v138 row_shr:2 row_mask:0xf bank_mask:0xf bound_ctrl:1
	s_nop 1
	v_add_f32_dpp v174, v138, v138 row_shr:4 row_mask:0xf bank_mask:0xf bound_ctrl:1
	s_nop 0
	s_nop 0
	v_mov_b32_dpp v130, v174 row_shr:8 row_mask:0xf bank_mask:0xf
	s_nop 0
	s_nop 1
	s_nop 0


	v_cvt_f32_f16_sdwa v164, v133 dst_sel:DWORD dst_unused:UNUSED_PAD src0_sel:WORD_1
	v_mov_b32_e32 v172, 0
	s_nop 0
	v_add_f32_dpp v133, v164, v164 row_shr:1 row_mask:0xf bank_mask:0xf bound_ctrl:1
	s_nop 0
	s_nop 0
	v_add_f32_dpp v133, v133, v133 row_shr:2 row_mask:0xf bank_mask:0xf bound_ctrl:1
	s_nop 1
	v_add_f32_dpp v173, v133, v133 row_shr:4 row_mask:0xf bank_mask:0xf bound_ctrl:1
	s_nop 0
	v_mov_b32_e32 v146, 0
	v_mov_b32_dpp v172, v173 row_shr:8 row_mask:0xf bank_mask:0xf
	s_nop 0
	s_nop 1
	s_nop 0


	v_cndmask_b32_e64 v146, 0, 1.0, s[96:97]
	v_add_f32_e32 v174, v174, v130
	s_nop 1
	v_mov_b32_dpp v138, v174 row_newbcast:15 row_mask:0xf bank_mask:0xf
	v_mul_f32_e32 v130, 0x3fb8aa3b, v174
	v_mul_f32_e32 v133, 0xbfb8aa3b, v174
	v_sub_f32_e32 v136, v174, v136
	v_sub_f32_e32 v138, v138, v174
	s_waitcnt vmcnt(0)
	v_mov_b32_e32 v174, v218
	v_mov_b32_e32 v175, v219
	v_mov_b32_e32 v176, v220
	v_mov_b32_e32 v177, v221
	v_add_f32_e32 v152, v135, v132
	s_nop 1
	v_mov_b32_dpp v171, v152 row_newbcast:15 row_mask:0xf bank_mask:0xf
	v_sub_f32_e32 v141, v152, v141
	v_mul_f32_e32 v132, 0x3fb8aa3b, v152
	v_mul_f32_e32 v141, 0x3fb8aa3b, v141
	v_add_f32_e32 v181, v173, v172
	s_nop 1
	v_mov_b32_dpp v168, v181 row_newbcast:15 row_mask:0xf bank_mask:0xf
	v_exp_f32_e32 v135, v132
	s_mov_b64 exec, s[96:97]
	ds_write_b32 v255, v135 offset:16436
	s_mov_b64 exec, -1
	v_mul_f32_e32 v132, 0xbfb8aa3b, v152
	v_exp_f32_e32 v183, v141
	v_sub_f32_e32 v141, v171, v152
	v_add_f32_e32 v152, v170, v134
	s_nop 1
	v_mov_b32_dpp v169, v152 row_newbcast:15 row_mask:0xf bank_mask:0xf
	v_mov_b32_e32 v170, v222
	v_mov_b32_e32 v171, v223
	v_mov_b32_e32 v172, v224
	v_mov_b32_e32 v173, v225
	v_add_f32_e32 v150, v167, v165
	s_nop 1
	v_mov_b32_dpp v166, v150 row_newbcast:15 row_mask:0xf bank_mask:0xf
	v_sub_f32_e32 v131, v150, v131
	v_mul_f32_e32 v131, 0x3fb8aa3b, v131
	v_exp_f32_e32 v167, v131
	v_sub_f32_e32 v131, v166, v150
	v_sub_f32_e32 v140, v152, v140
	v_mul_f32_e32 v131, 0x3fb8aa3b, v131
	v_mul_f32_e32 v140, 0x3fb8aa3b, v140
	v_exp_f32_e32 v185, v131
	v_add_f32_e32 v131, v163, v161
	s_nop 1
	v_mov_b32_dpp v162, v131 row_newbcast:15 row_mask:0xf bank_mask:0xf
	v_mul_f32_e32 v134, 0x3fb8aa3b, v152
	v_mul_f32_e32 v153, 0xbfb8aa3b, v152
	v_exp_f32_e32 v182, v140
	v_sub_f32_e32 v140, v169, v152
	v_mul_f32_e32 v151, 0x3fb8aa3b, v150
	v_mul_f32_e32 v152, 0xbfb8aa3b, v150
	v_mul_f32_e32 v150, 0x3fb8aa3b, v131
	v_mul_f32_e32 v161, 0xbfb8aa3b, v131
	v_sub_f32_e32 v160, v131, v160
	v_sub_f32_e32 v131, v162, v131
	v_mul_f32_e32 v131, 0x3fb8aa3b, v131
	v_exp_f32_e32 v184, v131
	v_add_f32_e32 v131, v159, v158
	s_nop 1
	v_mov_b32_dpp v157, v131 row_newbcast:15 row_mask:0xf bank_mask:0xf
	v_mul_f32_e32 v160, 0x3fb8aa3b, v160
	v_mul_f32_e32 v158, 0x3fb8aa3b, v131
	v_exp_f32_e32 v187, v161
	v_exp_f32_e32 v166, v160
	v_exp_f32_e32 v189, v158
	s_mov_b64 exec, s[96:97]
	ds_write_b32 v255, v189 offset:16420
	s_mov_b64 exec, -1
	v_mov_b32_e32 v158, v226
	v_mov_b32_e32 v159, v227
	v_mov_b32_e32 v160, v228
	v_mov_b32_e32 v161, v229
	v_mul_f32_e32 v162, 0xbfb8aa3b, v131
	v_sub_f32_e32 v148, v131, v156
	v_sub_f32_e32 v131, v157, v131
	v_mul_f32_e32 v131, 0x3fb8aa3b, v131
	v_exp_f32_e32 v191, v131
	v_add_f32_e32 v131, v139, v154
	s_nop 1
	v_mov_b32_dpp v155, v131 row_newbcast:15 row_mask:0xf bank_mask:0xf
	v_mul_f32_e32 v139, 0x3fb8aa3b, v131
	v_exp_f32_e32 v188, v139
	s_mov_b64 exec, s[96:97]
	ds_write_b32 v255, v188 offset:16416
	s_mov_b64 exec, -1
	v_mul_f32_e32 v139, 0xbfb8aa3b, v131
	v_sub_f32_e32 v137, v131, v137
	v_sub_f32_e32 v131, v155, v131
	v_mov_b32_e32 v154, v250
	v_mov_b32_e32 v155, v251
	v_mov_b32_e32 v156, v252
	v_mov_b32_e32 v157, v253
	s_cmpk_eq_i32 s26, 0xf0
	s_cbranch_scc1 .Lsc1_nopf
	s_sub_u32 s94, 0x8000, s22
	s_subb_u32 s95, 0, s23
	v_lshl_add_u64 v[250:251], v[142:143], 0, s[94:95]
	v_lshl_add_u64 v[218:219], s[8:9], 0, v[250:251]
	global_load_dwordx4 v[218:221], v[218:219], off
	v_lshl_add_u64 v[222:223], s[14:15], 0, v[250:251]
	global_load_dwordx4 v[222:225], v[222:223], off
	v_lshl_add_u64 v[226:227], s[14:15], 0, v[250:251]
	global_load_dwordx4 v[226:229], v[226:227], off offset:16
	v_lshl_add_u64 v[230:231], s[16:17], 0, v[250:251]
	global_load_dwordx4 v[230:233], v[230:231], off
	v_lshl_add_u64 v[234:235], s[18:19], 0, v[250:251]
	global_load_dwordx4 v[234:237], v[234:235], off
	v_lshl_add_u64 v[238:239], s[20:21], 0, v[250:251]
	global_load_dwordx4 v[238:241], v[238:239], off
	v_lshl_add_u64 v[242:243], s[8:9], 0, v[250:251]
	global_load_dwordx4 v[242:245], v[242:243], off offset:16
	v_lshl_add_u64 v[246:247], s[22:23], 0, v[250:251]
	global_load_dwordx4 v[246:249], v[246:247], off
.Lsc1_nopf:
	v_mul_f32_e32 v148, 0x3fb8aa3b, v148
	v_mul_f32_e32 v137, 0x3fb8aa3b, v137
	v_exp_f32_e32 v186, v162
	v_exp_f32_e32 v149, v148
	v_exp_f32_e32 v148, v137
	v_mul_f32_e32 v137, 0xbfb8aa3b, v181
	v_exp_f32_e32 v193, v137
	v_sub_f32_e32 v137, v181, v164
	v_mul_f32_e32 v136, 0x3fb8aa3b, v136
	v_mul_f32_e32 v137, 0x3fb8aa3b, v137
	v_exp_f32_e32 v136, v136
	v_exp_f32_e32 v137, v137
	v_mul_f32_e32 v131, 0x3fb8aa3b, v131
	v_exp_f32_e32 v190, v131
	v_exp_f32_e32 v153, v153
	v_exp_f32_e32 v152, v152
	v_mul_f32_e32 v141, 0x3fb8aa3b, v141
	v_mul_f32_e32 v140, 0x3fb8aa3b, v140
	v_exp_f32_e32 v192, v139
	v_exp_f32_e32 v141, v141
	v_exp_f32_e32 v140, v140
	v_exp_f32_e32 v133, v133
	v_exp_f32_e32 v132, v132
	v_sub_f32_e32 v139, v168, v181
	v_mul_f32_e32 v138, 0x3fb8aa3b, v138
	v_mul_f32_e32 v139, 0x3fb8aa3b, v139
	v_exp_f32_e32 v138, v138

	v_cvt_f32_f16_sdwa v163, v174 dst_sel:DWORD dst_unused:UNUSED_PAD src0_sel:WORD_1
	v_cvt_f32_f16_e32 v162, v174
	v_cvt_f32_f16_sdwa v165, v175 dst_sel:DWORD dst_unused:UNUSED_PAD src0_sel:WORD_1
	v_cvt_f32_f16_e32 v164, v175
	v_exp_f32_e32 v139, v139
	v_mul_f32_e32 v142, v148, v162
	v_mul_f32_e32 v143, v149, v163
	v_cvt_f32_f16_sdwa v149, v176 dst_sel:DWORD dst_unused:UNUSED_PAD src0_sel:WORD_1
	v_cvt_pk_f16_f32 v162, v142, v143
	v_mul_f32_e32 v142, v166, v164
	v_mul_f32_e32 v143, v167, v165
	v_cvt_f32_f16_e32 v148, v176
	v_cvt_f32_f16_sdwa v167, v177 dst_sel:DWORD dst_unused:UNUSED_PAD src0_sel:WORD_1
	v_cvt_f32_f16_e32 v166, v177
	v_cvt_pk_f16_f32 v163, v142, v143
	v_mul_f32_e32 v142, v182, v148
	v_mul_f32_e32 v143, v183, v149
	v_mul_f32_e32 v131, 0x3fb8aa3b, v181
	v_mul_f32_e32 v136, v136, v166
	v_mul_f32_e32 v137, v137, v167
	v_cvt_pk_f16_f32 v164, v142, v143
	v_cvt_pk_f16_f32 v165, v136, v137

	v_cvt_f32_f16_sdwa v137, v170 dst_sel:DWORD dst_unused:UNUSED_PAD src0_sel:WORD_1
	v_cvt_f32_f16_e32 v136, v170
	v_cvt_f32_f16_sdwa v143, v171 dst_sel:DWORD dst_unused:UNUSED_PAD src0_sel:WORD_1
	v_cvt_f32_f16_e32 v142, v171
	ds_write_b128 v147, v[162:165] offset:16
	v_mul_f32_e32 v148, v190, v136
	v_mul_f32_e32 v149, v191, v137
	v_fma_mixlo_f16 v163, v192, v170, 0 op_sel_hi:[0,1,0]
	v_mov_b32_e32 v136, v137
	v_mov_b32_e32 v137, v142
	v_cvt_pk_f16_f32 v162, v148, v149
	v_mul_f32_e32 v136, v186, v136
	v_mul_f32_e32 v137, v187, v137
	v_mul_f32_e32 v148, v184, v142
	v_mul_f32_e32 v149, v185, v143
	v_cvt_pk_f16_f32 v164, v136, v137
	v_cvt_f32_f16_sdwa v137, v172 dst_sel:DWORD dst_unused:UNUSED_PAD src0_sel:WORD_1
	v_cvt_f32_f16_e32 v136, v172
	v_pack_b32_f16 v166, v163, v164
	v_cvt_pk_f16_f32 v163, v148, v149
	v_exp_f32_e32 v130, v130
	s_mov_b64 exec, s[96:97]
	ds_write_b32 v255, v130 offset:16440
	s_mov_b64 exec, -1
	v_mov_b32_e32 v142, v143
	v_mov_b32_e32 v143, v136
	v_mul_f32_e32 v148, v140, v136
	v_mul_f32_e32 v149, v141, v137
	v_mul_f32_e32 v142, v152, v142
	v_mul_f32_e32 v143, v153, v143
	v_exp_f32_e32 v134, v134
	s_mov_b64 exec, s[96:97]
	ds_write_b32 v255, v134 offset:16432
	s_mov_b64 exec, -1
	v_cvt_pk_f16_f32 v165, v142, v143
	v_cvt_f32_f16_sdwa v143, v173 dst_sel:DWORD dst_unused:UNUSED_PAD src0_sel:WORD_1
	v_cvt_f32_f16_e32 v142, v173
	v_alignbit_b32 v167, v165, v164, 16
	v_cvt_pk_f16_f32 v164, v148, v149
	v_exp_f32_e32 v151, v151
	s_mov_b64 exec, s[96:97]
	ds_write_b32 v255, v151 offset:16428
	s_mov_b64 exec, -1
	v_mov_b32_e32 v136, v137
	v_mov_b32_e32 v137, v142
	v_exp_f32_e32 v150, v150
	s_mov_b64 exec, s[96:97]
	ds_write_b32 v255, v150 offset:16424
	s_mov_b64 exec, -1
	v_mul_f32_e32 v136, v132, v136
	v_mul_f32_e32 v137, v133, v137
	v_exp_f32_e32 v131, v131
	s_mov_b64 exec, s[96:97]
	ds_write_b32 v255, v131 offset:16444
	s_mov_b64 exec, -1
	v_cvt_pk_f16_f32 v136, v136, v137
	v_alignbit_b32 v168, v136, v165, 16
	v_lshrrev_b32_e32 v169, 16, v136
	v_mul_f32_e32 v136, v138, v142
	v_mul_f32_e32 v137, v139, v143

	v_cvt_f32_f16_sdwa v143, v159 dst_sel:DWORD dst_unused:UNUSED_PAD src0_sel:WORD_1
	v_cvt_pk_f16_f32 v165, v136, v137
	v_cvt_f32_f16_sdwa v137, v158 dst_sel:DWORD dst_unused:UNUSED_PAD src0_sel:WORD_1
	v_cvt_f32_f16_e32 v136, v158
	v_cvt_f32_f16_e32 v142, v159
	v_fma_mixhi_f16 v169, v193, v173, 0 op_sel:[0,1,0] op_sel_hi:[0,1,0]
	ds_write_b128 v147, v[166:169] offset:2064
	ds_write_b128 v147, v[162:165] offset:8208
	v_mul_f32_e32 v148, v190, v136
	v_mul_f32_e32 v149, v191, v137
	v_mov_b32_e32 v136, v137
	v_mov_b32_e32 v137, v142
	v_cvt_pk_f16_f32 v162, v148, v149
	v_mul_f32_e32 v136, v186, v136
	v_mul_f32_e32 v137, v187, v137
	v_mul_f32_e32 v148, v184, v142
	v_mul_f32_e32 v149, v185, v143
	v_cvt_pk_f16_f32 v159, v136, v137
	v_cvt_f32_f16_sdwa v137, v160 dst_sel:DWORD dst_unused:UNUSED_PAD src0_sel:WORD_1
	v_cvt_f32_f16_e32 v136, v160
	v_cvt_pk_f16_f32 v163, v148, v149
	v_fma_mixlo_f16 v158, v192, v158, 0 op_sel_hi:[0,1,0]
	v_lshlrev_b32_e32 v213, 4, v212
	v_mov_b32_e32 v142, v143
	v_mov_b32_e32 v143, v136
	v_mul_f32_e32 v140, v140, v136
	v_mul_f32_e32 v141, v141, v137
	v_mul_f32_e32 v142, v152, v142
	v_mul_f32_e32 v143, v153, v143
	v_cvt_pk_f16_f32 v164, v140, v141
	v_cvt_pk_f16_f32 v148, v142, v143
	v_cvt_f32_f16_sdwa v143, v161 dst_sel:DWORD dst_unused:UNUSED_PAD src0_sel:WORD_1
	v_cvt_f32_f16_e32 v142, v161

	v_cvt_f32_f16_sdwa v141, v157 dst_sel:DWORD dst_unused:UNUSED_PAD src0_sel:WORD_1
	v_cvt_f32_f16_e32 v140, v157
	v_pack_b32_f16 v166, v158, v159
	v_mov_b32_e32 v136, v137
	v_mov_b32_e32 v137, v142
	v_alignbit_b32 v167, v148, v159, 16
	v_mul_f32_e32 v132, v132, v136
	v_mul_f32_e32 v133, v133, v137
	v_cvt_f32_f16_sdwa v137, v155 dst_sel:DWORD dst_unused:UNUSED_PAD src0_sel:WORD_1
	v_cvt_pk_f16_f32 v132, v132, v133
	v_alignbit_b32 v168, v132, v148, 16
	v_lshrrev_b32_e32 v169, 16, v132
	v_mul_f32_e32 v132, v138, v142
	v_mul_f32_e32 v133, v139, v143
	v_cvt_f32_f16_e32 v136, v155
	v_cvt_pk_f16_f32 v165, v132, v133
	v_cvt_f32_f16_sdwa v133, v154 dst_sel:DWORD dst_unused:UNUSED_PAD src0_sel:WORD_1
	v_cvt_f32_f16_e32 v132, v154
	v_cvt_f32_f16_sdwa v139, v156 dst_sel:DWORD dst_unused:UNUSED_PAD src0_sel:WORD_1
	v_cvt_f32_f16_e32 v138, v156
	v_mul_f32_e32 v136, v150, v136
	v_mul_f32_e32 v137, v151, v137
	v_mul_f32_e32 v132, v188, v132
	v_mul_f32_e32 v133, v189, v133
	v_mul_f32_e32 v130, v130, v140
	v_mul_f32_e32 v131, v131, v141
	v_mul_f32_e32 v134, v134, v138
	v_mul_f32_e32 v135, v135, v139
	v_fma_mixhi_f16 v169, v193, v161, 0 op_sel:[0,1,0] op_sel_hi:[0,1,0]
	v_cvt_pk_f16_f32 v132, v132, v133
	v_cvt_pk_f16_f32 v133, v136, v137
	v_cvt_pk_f16_f32 v134, v134, v135
	v_cvt_pk_f16_f32 v135, v130, v131
	v_and_b32_e32 v130, 0xfffffe00, v213
	v_and_b32_e32 v131, 16, v212
	ds_write_b128 v147, v[166:169] offset:4112
	ds_write_b128 v147, v[162:165] offset:10256
	ds_write_b128 v147, v[132:135] offset:6160
	v_or3_b32 v130, v130, v131, v180
	s_waitcnt lgkmcnt(0)
	v_add_u32_e32 v142, s36, v130
	ds_read_b128 v[130:133], v142
	ds_read_b128 v[134:137], v142 offset:2048
	ds_read_b128 v[138:141], v142 offset:1024
	ds_read_b128 v[148:151], v142 offset:3072
	ds_read_b128 v[156:159], v142 offset:4096
	ds_read_b128 v[160:163], v142 offset:5120
	ds_read_b128 v[164:167], v142 offset:6144
	ds_read_b128 v[168:171], v142 offset:7168
	s_waitcnt lgkmcnt(6)
	v_mfma_f32_16x16x32_f16 v[152:155], v[130:133], v[134:137], 0
	v_lshlrev_b32_e32 v208, 2, v179
	v_lshl_add_u32 v215, v144, 2, s36
	v_cmp_gt_i32_e32 vcc, v208, v144
	s_waitcnt lgkmcnt(3)
	v_mfma_f32_16x16x32_f16 v[130:133], v[130:133], v[156:159], 0
	v_lshl_add_u32 v143, v179, 8, v215
	v_or_b32_e32 v211, 1, v208
	v_or_b32_e32 v209, 2, v208
	s_waitcnt lgkmcnt(1)
	v_mfma_f32_16x16x32_f16 v[134:137], v[164:167], v[134:137], 0
	v_or_b32_e32 v210, 3, v208
	v_mfma_f32_16x16x32_f16 v[156:159], v[164:167], v[156:159], 0
	v_mfma_f32_16x16x32_f16 v[130:133], v[138:141], v[160:163], v[130:133]
	v_mfma_f32_16x16x32_f16 v[152:155], v[138:141], v[148:151], v[152:155]
	s_waitcnt lgkmcnt(0)
	v_mfma_f32_16x16x32_f16 v[134:137], v[168:171], v[148:151], v[134:137]
	s_nop 4
	v_cvt_f16_f32_e32 v130, v130
	v_cvt_f16_f32_e32 v131, v131
	v_cndmask_b32_e32 v142, 0, v152, vcc
	v_mfma_f32_16x16x32_f16 v[138:141], v[168:171], v[160:163], v[156:159]
	v_cndmask_b32_e32 v130, 0, v130, vcc
	v_cvt_f16_f32_e32 v134, v134
	v_cvt_f16_f32_e32 v135, v135
	v_cmp_lt_i32_e32 vcc, v208, v144
	ds_write_b32 v143, v142 offset:14336
	s_nop 2
	v_cvt_f16_f32_e32 v138, v138
	v_cvt_f16_f32_e32 v139, v139
	v_cndmask_b32_e64 v142, v153, 0, vcc
	v_lshl_add_u32 v143, v211, 6, v215
	v_cndmask_b32_e64 v134, v134, 0, vcc
	v_cndmask_b32_e64 v138, v138, 0, vcc
	ds_write_b32 v143, v142 offset:14336
	v_cndmask_b32_e64 v142, v131, 0, vcc
	v_cmp_lt_i32_e32 vcc, v211, v144
	v_lshl_add_u32 v143, v209, 6, v215
	v_cvt_f16_f32_e32 v132, v132
	v_cndmask_b32_e64 v135, v135, 0, vcc
	v_cndmask_b32_e64 v139, v139, 0, vcc
	v_cmp_gt_i32_e32 vcc, v209, v144
	v_add_u32_e32 v161, s36, v180
	v_pack_b32_f16 v130, v130, v142
	v_cndmask_b32_e32 v131, 0, v154, vcc
	ds_write_b32 v143, v131 offset:14336
	v_cvt_f16_f32_e32 v131, v136
	v_cvt_f16_f32_e32 v136, v140
	v_cndmask_b32_e32 v132, 0, v132, vcc
	v_cmp_lt_i32_e32 vcc, v209, v144
	v_lshl_add_u32 v143, v210, 6, v215
	s_nop 0
	v_cndmask_b32_e64 v140, v131, 0, vcc
	v_cvt_f16_f32_e32 v131, v133
	v_cndmask_b32_e64 v136, v136, 0, vcc
	v_cmp_gt_i32_e32 vcc, v210, v144
	s_nop 1
	v_cndmask_b32_e32 v131, 0, v131, vcc
	v_pack_b32_f16 v131, v132, v131
	v_cvt_f16_f32_e32 v132, v137
	v_cvt_f16_f32_e32 v137, v141
	v_cndmask_b32_e32 v133, 0, v155, vcc
	v_cmp_lt_i32_e32 vcc, v210, v144
	ds_write_b32 v143, v133 offset:14336
	s_nop 0
	v_cndmask_b32_e64 v132, v132, 0, vcc
	v_pack_b32_f16 v133, v140, v132
	v_pack_b32_f16 v132, v134, v135
	v_cndmask_b32_e64 v134, v137, 0, vcc
	v_pack_b32_f16 v135, v136, v134
	v_lshlrev_b32_e32 v136, 3, v179
	v_add_u32_e32 v160, v161, v136
	v_pack_b32_f16 v134, v138, v139
	ds_write_b64 v160, v[130:131] offset:15872
	ds_write2st64_b64 v160, v[132:133], v[134:135] offset0:4 offset1:5
	s_waitcnt lgkmcnt(0)
	v_cmp_gt_u32_e32 vcc, 16, v212
	s_and_saveexec_b64 s[0:1], vcc
	s_cbranch_execz .LBB0_1289
	v_mov_b32_e32 v179, s36
	v_add_u32_e32 v214, 0x3800, v179
	ds_read2_b64 v[150:153], v214 offset0:8 offset1:16
	ds_read_b128 v[130:133], v179 offset:14528
	ds_read_b128 v[154:157], v179 offset:14592
	v_cmp_eq_u32_e32 vcc, 0, v144
	s_waitcnt lgkmcnt(2)
	v_mov_b32_e32 v136, v152
	v_cndmask_b32_e64 v148, 0, 1.0, vcc
	v_cmp_eq_u32_e32 vcc, 3, v144
	v_mov_b32_e32 v137, v150
	s_waitcnt lgkmcnt(1)
	v_mov_b32_e32 v158, v131
	v_cndmask_b32_e64 v133, 0, 1.0, vcc
	v_cmp_eq_u32_e32 vcc, 1, v144
	v_fma_f32 v147, -v148, v130, v133
	v_mov_b32_e32 v159, v132
	v_cndmask_b32_e64 v135, 0, 1.0, vcc
	v_cmp_eq_u32_e32 vcc, 2, v144
	s_waitcnt lgkmcnt(0)
	v_mov_b32_e32 v175, v154
	v_mov_b32_e32 v205, v156
	v_cndmask_b32_e64 v134, 0, 1.0, vcc
	v_fma_f32 v150, -v148, v136, v134
	v_fma_f32 v151, -v148, v137, v135
	ds_read_b128 v[140:143], v179 offset:15296
	ds_read_b128 v[136:139], v179 offset:15312
	ds_read_b128 v[162:165], v179 offset:14656
	ds_read_b128 v[130:133], v179 offset:14720
	ds_read_b128 v[166:169], v179 offset:14784
	ds_read_b128 v[170:173], v179 offset:14800
	v_cmp_eq_u32_e32 vcc, 4, v144
	s_waitcnt lgkmcnt(3)
	v_mov_b32_e32 v207, v164
	s_waitcnt lgkmcnt(2)
	v_mov_b32_e32 v206, v132
	v_cndmask_b32_e64 v135, 0, 1.0, vcc
	v_cmp_eq_u32_e32 vcc, 7, v144
	s_waitcnt lgkmcnt(1)
	v_mov_b32_e32 v174, v166
	v_mov_b32_e32 v154, v167
	v_cndmask_b32_e64 v134, 0, 1.0, vcc
	v_fma_f32 v134, -v148, v174, v134
	v_fma_f32 v135, -v148, v175, v135
	v_mov_b32_e32 v204, v168
	v_mov_b32_e32 v156, v169
	v_cmp_eq_u32_e32 vcc, 5, v144
	ds_read2_b64 v[166:169], v214 offset0:42 offset1:50
	v_fma_f32 v176, -v151, v154, v134
	v_fma_f32 v177, -v151, v155, v135
	v_cndmask_b32_e64 v135, 0, 1.0, vcc
	v_cmp_eq_u32_e32 vcc, 6, v144
	v_mov_b32_e32 v154, v130
	v_mov_b32_e32 v155, v162
	v_mov_b32_e32 v162, v131
	v_mov_b32_e32 v164, v133
	s_waitcnt lgkmcnt(0)
	v_mov_b32_e32 v167, v172
	ds_read_b128 v[172:175], v179 offset:14848
	ds_read_b128 v[180:183], v179 offset:14864
	ds_read_b128 v[130:133], v179 offset:14944
	ds_read_b128 v[184:187], v179 offset:14976
	ds_read_b128 v[188:191], v179 offset:14912
	ds_read_b128 v[192:195], v179 offset:14928
	v_cndmask_b32_e64 v134, 0, 1.0, vcc
	v_fma_f32 v134, -v148, v154, v134
	v_fma_f32 v135, -v148, v155, v135
	v_cmp_eq_u32_e32 vcc, 10, v144
	v_mov_b32_e32 v149, v151
	ds_read_b128 v[196:199], v179 offset:14992
	ds_read_b128 v[200:203], v179 offset:15040
	s_waitcnt lgkmcnt(5)
	v_cndmask_b32_e64 v131, 0, 1.0, vcc
	s_waitcnt lgkmcnt(4)
	v_mul_f32_e32 v132, v148, v184
	v_mul_f32_e32 v133, v149, v185
	v_fma_f32 v162, -v151, v162, v134
	v_fma_f32 v163, -v151, v163, v135
	v_sub_f32_e32 v131, v131, v132
	v_sub_f32_e32 v131, v131, v133
	ds_read2_b64 v[132:135], v214 offset0:84 offset1:110
	v_cmp_eq_u32_e32 vcc, 11, v144
	v_mov_b32_e32 v152, v151
	s_waitcnt lgkmcnt(1)
	v_mov_b32_e32 v184, v201
	s_waitcnt lgkmcnt(0)
	v_cndmask_b32_e64 v135, 0, 1.0, vcc
	v_fma_f32 v154, -v148, v200, v135
	v_mov_b32_e32 v185, v151
	v_mov_b32_e32 v155, v150
	v_fma_f32 v152, -v152, v184, v154
	v_fma_f32 v153, -v153, v185, v155
	v_mov_b32_e32 v154, v151
	v_mov_b32_e32 v155, v153
	v_mul_f32_e32 v154, v158, v154
	v_mul_f32_e32 v155, v159, v155
	v_fma_f32 v158, -v153, v204, v176
	v_fma_f32 v159, -v153, v205, v177
	v_sub_f32_e32 v135, v147, v154
	v_sub_f32_e32 v154, v135, v155
	v_fma_f32 v156, -v154, v156, v158
	v_fma_f32 v157, -v154, v157, v159
	v_fma_f32 v158, -v153, v206, v162
	v_fma_f32 v159, -v153, v207, v163
	v_mov_b32_e32 v162, v153
	v_mov_b32_e32 v163, v154
	v_mov_b32_e32 v216, v168
	v_mov_b32_e32 v217, v166
	v_fma_f32 v158, -v154, v164, v158
	v_fma_f32 v159, -v154, v165, v159
	v_mul_f32_e32 v162, v162, v186
	v_mul_f32_e32 v163, v163, v187
	v_fma_f32 v158, -v216, v157, v158
	v_fma_f32 v159, -v217, v157, v159
	v_sub_f32_e32 v131, v131, v162
	v_sub_f32_e32 v131, v131, v163
	v_mov_b32_e32 v162, v157
	v_mov_b32_e32 v163, v159
	v_mul_f32_e32 v162, v162, v196
	v_mul_f32_e32 v163, v163, v197
	v_mov_b32_e32 v166, v171
	v_sub_f32_e32 v131, v131, v162
	v_sub_f32_e32 v131, v131, v163
	ds_read_b128 v[162:165], v179 offset:15056
	ds_read_b128 v[184:187], v179 offset:15072
	v_fma_f32 v135, -v157, v170, v156
	v_mov_b32_e32 v155, v157
	v_mov_b32_e32 v170, v203
	s_waitcnt lgkmcnt(1)
	v_mov_b32_e32 v171, v162
	v_fma_f32 v147, -v153, v202, v152
	v_mul_f32_e32 v170, v154, v170
	v_mul_f32_e32 v171, v155, v171
	v_mov_b32_e32 v168, v159
	v_sub_f32_e32 v147, v147, v170
	v_sub_f32_e32 v162, v147, v171
	v_mov_b32_e32 v170, v163
	v_mov_b32_e32 v171, v159
	v_mov_b32_e32 v163, v158
	v_fma_f32 v196, -v168, v170, v162
	v_fma_f32 v197, -v169, v171, v163
	v_mov_b32_e32 v162, v159
	v_mov_b32_e32 v163, v197
	v_mul_f32_e32 v162, v166, v162
	v_mul_f32_e32 v163, v167, v163
	v_mov_b32_e32 v200, v197
	v_sub_f32_e32 v135, v135, v162
	v_sub_f32_e32 v201, v135, v163
	v_mul_f32_e32 v162, v200, v198
	v_mul_f32_e32 v163, v201, v199
	v_cmp_eq_u32_e32 vcc, 8, v144
	v_sub_f32_e32 v131, v131, v162
	v_sub_f32_e32 v131, v131, v163
	v_cndmask_b32_e64 v163, 0, 1.0, vcc
	v_cmp_eq_u32_e32 vcc, 9, v144
	v_mov_b32_e32 v166, v188
	v_mov_b32_e32 v167, v172
	v_cndmask_b32_e64 v162, 0, 1.0, vcc
	v_fma_f32 v162, -v148, v166, v162
	v_fma_f32 v163, -v148, v167, v163
	v_mov_b32_e32 v172, v189
	v_fma_f32 v162, -v151, v172, v162
	v_fma_f32 v163, -v151, v173, v163
	v_mov_b32_e32 v166, v190
	v_mov_b32_e32 v167, v174
	v_fma_f32 v162, -v153, v166, v162
	v_fma_f32 v163, -v153, v167, v163
	v_mov_b32_e32 v174, v191
	v_fma_f32 v162, -v154, v174, v162
	v_fma_f32 v163, -v154, v175, v163
	v_mov_b32_e32 v166, v192
	v_mov_b32_e32 v167, v180
	v_fma_f32 v162, -v157, v166, v162
	v_fma_f32 v163, -v157, v167, v163
	v_mov_b32_e32 v180, v193
	v_fma_f32 v162, -v159, v180, v162
	v_fma_f32 v163, -v159, v181, v163
	v_mov_b32_e32 v166, v194
	v_mov_b32_e32 v167, v182
	v_fma_f32 v162, -v197, v166, v162
	v_fma_f32 v163, -v197, v167, v163
	v_mov_b32_e32 v182, v195
	v_mov_b32_e32 v188, v201
	v_fma_f32 v190, -v182, v188, v162
	v_fma_f32 v191, -v183, v188, v163
	v_fma_f32 v135, -v197, v164, v196
	v_fma_f32 v193, -v130, v191, v190
	v_mov_b32_e32 v192, v191
	v_mov_b32_e32 v162, v201
	v_mov_b32_e32 v163, v191
	v_mov_b32_e32 v164, v165
	s_waitcnt lgkmcnt(0)
	v_mov_b32_e32 v165, v184
	v_mul_f32_e32 v132, v132, v192
	v_mul_f32_e32 v133, v133, v193
	v_mul_f32_e32 v162, v162, v164
	v_mul_f32_e32 v163, v163, v165
	v_sub_f32_e32 v131, v131, v132
	v_sub_f32_e32 v132, v135, v162
	v_sub_f32_e32 v135, v132, v163
	v_sub_f32_e32 v133, v131, v133
	v_mov_b32_e32 v162, v185
	v_mov_b32_e32 v163, v186
	v_mov_b32_e32 v132, v193
	v_mul_f32_e32 v162, v162, v132
	v_mul_f32_e32 v163, v163, v133
	v_cmp_eq_u32_e32 vcc, 12, v144
	v_sub_f32_e32 v131, v135, v162
	v_sub_f32_e32 v192, v131, v163
	ds_read_b128 v[162:165], v179 offset:15328
	ds_read_b128 v[166:169], v179 offset:15344
	ds_read_b128 v[170:173], v179 offset:15104
	ds_read_b128 v[174:177], v179 offset:15120
	ds_read_b128 v[180:183], v179 offset:15136
	v_cndmask_b32_e64 v147, 0, 1.0, vcc
	v_mov_b32_e32 v184, v140
	s_waitcnt lgkmcnt(2)
	v_mov_b32_e32 v185, v170
	v_fma_f32 v146, -v148, v184, v146
	v_fma_f32 v147, -v148, v185, v147
	v_mov_b32_e32 v170, v141
	v_fma_f32 v140, -v151, v170, v146
	v_fma_f32 v141, -v151, v171, v147
	v_mov_b32_e32 v146, v142
	v_mov_b32_e32 v147, v172
	v_fma_f32 v140, -v146, v153, v140
	v_fma_f32 v141, -v147, v153, v141
	v_mov_b32_e32 v172, v143
	v_fma_f32 v140, -v172, v154, v140
	v_fma_f32 v141, -v173, v154, v141
	v_mov_b32_e32 v142, v136
	s_waitcnt lgkmcnt(1)
	v_mov_b32_e32 v143, v174
	v_fma_f32 v140, -v157, v142, v140
	v_fma_f32 v141, -v157, v143, v141
	v_mov_b32_e32 v174, v137
	v_fma_f32 v136, -v159, v174, v140
	v_fma_f32 v137, -v159, v175, v141
	v_mov_b32_e32 v140, v138
	v_mov_b32_e32 v141, v176
	v_fma_f32 v136, -v140, v197, v136
	v_fma_f32 v137, -v141, v197, v137
	v_mov_b32_e32 v176, v139
	v_fma_f32 v140, -v176, v188, v136
	v_fma_f32 v141, -v177, v188, v137
	v_mov_b32_e32 v142, v162
	s_waitcnt lgkmcnt(0)
	v_mov_b32_e32 v143, v180
	v_fma_f32 v140, -v142, v191, v140
	v_fma_f32 v141, -v143, v191, v141
	v_mov_b32_e32 v180, v163
	v_fma_f32 v140, -v180, v132, v140
	v_fma_f32 v141, -v181, v132, v141
	v_mov_b32_e32 v142, v164
	v_mov_b32_e32 v143, v182
	v_mov_b32_e32 v146, v133
	v_fma_f32 v140, -v142, v146, v140
	v_fma_f32 v141, -v143, v146, v141
	v_mov_b32_e32 v182, v165
	ds_read_b128 v[136:139], v179 offset:15168
	v_fma_f32 v194, -v182, v192, v140
	v_fma_f32 v195, -v183, v192, v141
	ds_read_b128 v[140:143], v179 offset:15184
	ds_read_b128 v[162:165], v179 offset:15200
	ds_read_b128 v[170:173], v179 offset:15232
	v_cmp_eq_u32_e32 vcc, 13, v144
	ds_read_b128 v[174:177], v179 offset:15248
	s_waitcnt lgkmcnt(4)
	v_mov_b32_e32 v183, v136
	v_cndmask_b32_e64 v181, 0, 1.0, vcc
	v_cmp_eq_u32_e32 vcc, 14, v144
	s_waitcnt lgkmcnt(1)
	v_mov_b32_e32 v182, v170
	v_mov_b32_e32 v136, v171
	v_cndmask_b32_e64 v180, 0, 1.0, vcc
	v_fma_f32 v198, -v148, v182, v180
	v_fma_f32 v199, -v148, v183, v181
	v_fma_f32 v136, -v151, v136, v198
	v_fma_f32 v137, -v151, v137, v199
	v_mov_b32_e32 v170, v172
	v_mov_b32_e32 v171, v138
	v_fma_f32 v136, -v153, v170, v136
	v_fma_f32 v137, -v153, v171, v137
	v_mov_b32_e32 v138, v173
	ds_read_b128 v[180:183], v179 offset:15264
	ds_read_b128 v[184:187], v179 offset:15280
	v_fma_f32 v136, -v154, v138, v136
	v_fma_f32 v137, -v154, v139, v137
	s_waitcnt lgkmcnt(2)
	v_mov_b32_e32 v138, v174
	v_mov_b32_e32 v139, v140
	v_fma_f32 v136, -v157, v138, v136
	v_fma_f32 v137, -v157, v139, v137
	v_mov_b32_e32 v140, v175
	v_fma_f32 v136, -v159, v140, v136
	v_fma_f32 v137, -v159, v141, v137
	v_mov_b32_e32 v138, v176
	v_mov_b32_e32 v139, v142
	v_fma_f32 v136, -v197, v138, v136
	v_fma_f32 v137, -v197, v139, v137
	v_mov_b32_e32 v142, v177
	v_fma_f32 v136, -v188, v142, v136
	v_fma_f32 v137, -v188, v143, v137
	s_waitcnt lgkmcnt(1)
	v_mov_b32_e32 v138, v180
	v_mov_b32_e32 v139, v162
	v_fma_f32 v136, -v191, v138, v136
	v_fma_f32 v137, -v191, v139, v137
	v_mov_b32_e32 v162, v181
	v_fma_f32 v136, -v132, v162, v136
	v_fma_f32 v137, -v132, v163, v137
	v_mov_b32_e32 v138, v182
	v_mov_b32_e32 v139, v164
	v_fma_f32 v136, -v146, v138, v136
	v_fma_f32 v137, -v146, v139, v137
	v_mov_b32_e32 v164, v183
	v_fma_f32 v136, -v192, v164, v136
	v_fma_f32 v137, -v192, v165, v137
	s_waitcnt lgkmcnt(0)
	v_mov_b32_e32 v138, v184
	v_mov_b32_e32 v139, v134
	v_fma_f32 v136, -v138, v195, v136
	v_fma_f32 v137, -v139, v195, v137
	v_mov_b32_e32 v138, v167
	v_fma_f32 v135, -v185, v137, v136
	v_mov_b32_e32 v139, v168
	v_mov_b32_e32 v134, v137
	v_cvt_f16_f32_e32 v132, v191
	v_fma_f32 v131, -v166, v195, v194
	v_mul_f32_e32 v138, v138, v134
	v_mul_f32_e32 v139, v139, v135
	v_cvt_pk_f16_f32 v134, v195, v137
	v_sub_f32_e32 v131, v131, v138
	v_sub_f32_e32 v131, v131, v139
	v_cvt_pk_f16_f32 v139, v197, v201
	v_cvt_pk_f16_f32 v138, v157, v159
	v_cvt_pk_f16_f32 v137, v153, v154
	v_cvt_pk_f16_f32 v136, v148, v151
	v_cvt_pk_f16_f32 v135, v135, v131
	v_cvt_pk_f16_f32 v133, v133, v192
	v_fma_mixhi_f16 v132, -v130, v191, v190
	ds_write_b128 v161, v[136:139] offset:15360
	ds_write_b128 v161, v[132:135] offset:15376
	s_branch .LBB0_1289
